# GEMM K-loops: A-half LDS-DMA pair moved from the 6-request load segment to the following 2-request segment (counted wait 8->6)
# speedup vs baseline: 1.0065x; 1.0041x over previous
.LBB0_115:
	ds_read_b128 v[130:133], v206
	ds_read_b128 v[134:137], v206 offset:1024
	ds_read_b128 v[138:141], v206 offset:2048
	ds_read_b128 v[142:145], v206 offset:3072
	ds_read_b128 v[146:149], v207
	ds_read_b128 v[150:153], v207 offset:1024
	ds_read_b128 v[154:157], v207 offset:2048
	ds_read_b128 v[158:161], v207 offset:3072
	s_add_i32 s10, vcc_hi, 0x80
	s_cmp_eq_u32 s1, 28
	s_cselect_b32 s12, s57, s10
	s_cselect_b32 s95, vcc_lo, s0
	s_or_b32 s59, s12, 0x80
	s_mov_b32 m0, s86
	ds_read_b128 v[162:165], v208
	ds_read_b128 v[166:169], v208 offset:1024
	ds_read_b128 v[170:173], v208 offset:2048
	ds_read_b128 v[178:181], v208 offset:3072
	ds_read_b128 v[214:217], v208 offset:4096
	ds_read_b128 v[218:221], v208 offset:5120
	ds_read_b128 v[222:225], v208 offset:6144
	ds_read_b128 v[226:229], v208 offset:7168
	buffer_load_dwordx4 v196, s[68:71], vcc_hi offen lds
	s_mov_b32 m0, s87
	s_nop 0
	buffer_load_dwordx4 v198, s[68:71], vcc_hi offen lds
	s_waitcnt vmcnt(8)
	s_waitcnt lgkmcnt(0)
	s_barrier
	s_setprio 1
	s_waitcnt lgkmcnt(7)
	v_mfma_f32_16x16x32_bf16 v[126:129], v[130:133], v[162:165], v[126:129]
	v_mfma_f32_16x16x32_bf16 v[122:125], v[138:141], v[162:165], v[122:125]
	s_waitcnt lgkmcnt(5)
	v_mfma_f32_16x16x32_bf16 v[110:113], v[130:133], v[170:173], v[110:113]
	v_mfma_f32_16x16x32_bf16 v[106:109], v[138:141], v[170:173], v[106:109]
	s_waitcnt lgkmcnt(3)
	v_mfma_f32_16x16x32_bf16 v[94:97], v[130:133], v[214:217], v[94:97]
	v_mfma_f32_16x16x32_bf16 v[90:93], v[138:141], v[214:217], v[90:93]
	s_waitcnt lgkmcnt(1)
	v_mfma_f32_16x16x32_bf16 v[78:81], v[130:133], v[222:225], v[78:81]
	v_mfma_f32_16x16x32_bf16 v[74:77], v[138:141], v[222:225], v[74:77]
	v_mfma_f32_16x16x32_bf16 v[126:129], v[134:137], v[166:169], v[126:129]
	v_mfma_f32_16x16x32_bf16 v[122:125], v[142:145], v[166:169], v[122:125]
	v_mfma_f32_16x16x32_bf16 v[110:113], v[134:137], v[178:181], v[110:113]
	v_mfma_f32_16x16x32_bf16 v[106:109], v[142:145], v[178:181], v[106:109]
	v_mfma_f32_16x16x32_bf16 v[94:97], v[134:137], v[218:221], v[94:97]
	v_mfma_f32_16x16x32_bf16 v[90:93], v[142:145], v[218:221], v[90:93]
	s_waitcnt lgkmcnt(0)
	v_mfma_f32_16x16x32_bf16 v[78:81], v[134:137], v[226:229], v[78:81]
	v_mfma_f32_16x16x32_bf16 v[74:77], v[142:145], v[226:229], v[74:77]
	s_setprio 0
	s_setprio 1
	v_mfma_f32_16x16x32_bf16 v[118:121], v[146:149], v[162:165], v[118:121]
	v_mfma_f32_16x16x32_bf16 v[114:117], v[154:157], v[162:165], v[114:117]
	v_mfma_f32_16x16x32_bf16 v[102:105], v[146:149], v[170:173], v[102:105]
	v_mfma_f32_16x16x32_bf16 v[98:101], v[154:157], v[170:173], v[98:101]
	v_mfma_f32_16x16x32_bf16 v[86:89], v[146:149], v[214:217], v[86:89]
	v_mfma_f32_16x16x32_bf16 v[82:85], v[154:157], v[214:217], v[82:85]
	v_mfma_f32_16x16x32_bf16 v[70:73], v[146:149], v[222:225], v[70:73]
	v_mfma_f32_16x16x32_bf16 v[66:69], v[154:157], v[222:225], v[66:69]
	v_mfma_f32_16x16x32_bf16 v[118:121], v[150:153], v[166:169], v[118:121]
	v_mfma_f32_16x16x32_bf16 v[114:117], v[158:161], v[166:169], v[114:117]
	v_mfma_f32_16x16x32_bf16 v[102:105], v[150:153], v[178:181], v[102:105]
	v_mfma_f32_16x16x32_bf16 v[98:101], v[158:161], v[178:181], v[98:101]
	v_mfma_f32_16x16x32_bf16 v[86:89], v[150:153], v[218:221], v[86:89]
	v_mfma_f32_16x16x32_bf16 v[82:85], v[158:161], v[218:221], v[82:85]
	v_mfma_f32_16x16x32_bf16 v[70:73], v[150:153], v[226:229], v[70:73]
	v_mfma_f32_16x16x32_bf16 v[66:69], v[158:161], v[226:229], v[66:69]
	s_setprio 0
	s_barrier
	s_mov_b32 m0, s62
	s_mov_b32 s10, s70
	s_mov_b32 s11, s71
	ds_read_b128 v[162:165], v208 offset:16384
	ds_read_b128 v[166:169], v208 offset:17408
	ds_read_b128 v[170:173], v208 offset:18432
	ds_read_b128 v[178:181], v208 offset:19456
	ds_read_b128 v[214:217], v208 offset:20480
	ds_read_b128 v[218:221], v208 offset:21504
	ds_read_b128 v[222:225], v208 offset:22528
	ds_read_b128 v[226:229], v208 offset:23552
	buffer_load_dwordx4 v192, s[8:11], s95 offen lds
	s_mov_b32 m0, s63
	s_add_i32 s13, s95, 0x80000
	buffer_load_dwordx4 v193, s[8:11], s95 offen lds
	s_mov_b32 m0, s64
	s_nop 0
	buffer_load_dwordx4 v192, s[8:11], s13 offen lds
	s_mov_b32 m0, s65
	s_nop 0
	buffer_load_dwordx4 v193, s[8:11], s13 offen lds
	s_waitcnt vmcnt(6)
	s_waitcnt lgkmcnt(0)
	s_barrier
	s_setprio 1
	s_waitcnt lgkmcnt(7)
	v_mfma_f32_16x16x32_bf16 v[62:65], v[130:133], v[162:165], v[62:65]
	v_mfma_f32_16x16x32_bf16 v[58:61], v[138:141], v[162:165], v[58:61]
	s_waitcnt lgkmcnt(5)
	v_mfma_f32_16x16x32_bf16 v[46:49], v[130:133], v[170:173], v[46:49]
	v_mfma_f32_16x16x32_bf16 v[42:45], v[138:141], v[170:173], v[42:45]
	s_waitcnt lgkmcnt(3)
	v_mfma_f32_16x16x32_bf16 v[22:25], v[130:133], v[214:217], v[22:25]
	v_mfma_f32_16x16x32_bf16 v[18:21], v[138:141], v[214:217], v[18:21]
	s_waitcnt lgkmcnt(1)
	v_mfma_f32_16x16x32_bf16 v[6:9], v[130:133], v[222:225], v[6:9]
	v_mfma_f32_16x16x32_bf16 v[2:5], v[138:141], v[222:225], v[2:5]
	v_mfma_f32_16x16x32_bf16 v[62:65], v[134:137], v[166:169], v[62:65]
	v_mfma_f32_16x16x32_bf16 v[58:61], v[142:145], v[166:169], v[58:61]
	v_mfma_f32_16x16x32_bf16 v[46:49], v[134:137], v[178:181], v[46:49]
	v_mfma_f32_16x16x32_bf16 v[42:45], v[142:145], v[178:181], v[42:45]
	v_mfma_f32_16x16x32_bf16 v[22:25], v[134:137], v[218:221], v[22:25]
	v_mfma_f32_16x16x32_bf16 v[18:21], v[142:145], v[218:221], v[18:21]
	s_waitcnt lgkmcnt(0)
	v_mfma_f32_16x16x32_bf16 v[6:9], v[134:137], v[226:229], v[6:9]
	v_mfma_f32_16x16x32_bf16 v[2:5], v[142:145], v[226:229], v[2:5]
	s_setprio 0
	s_setprio 1
	v_mfma_f32_16x16x32_bf16 v[54:57], v[146:149], v[162:165], v[54:57]
	v_mfma_f32_16x16x32_bf16 v[50:53], v[154:157], v[162:165], v[50:53]
	v_mfma_f32_16x16x32_bf16 v[30:33], v[146:149], v[170:173], v[30:33]
	v_mfma_f32_16x16x32_bf16 v[26:29], v[154:157], v[170:173], v[26:29]
	v_mfma_f32_16x16x32_bf16 v[34:37], v[146:149], v[214:217], v[34:37]
	v_mfma_f32_16x16x32_bf16 v[38:41], v[154:157], v[214:217], v[38:41]
	v_mfma_f32_16x16x32_bf16 v[10:13], v[146:149], v[222:225], v[10:13]
	v_mfma_f32_16x16x32_bf16 v[14:17], v[154:157], v[222:225], v[14:17]
	v_mfma_f32_16x16x32_bf16 v[54:57], v[150:153], v[166:169], v[54:57]
	v_mfma_f32_16x16x32_bf16 v[50:53], v[158:161], v[166:169], v[50:53]
	v_mfma_f32_16x16x32_bf16 v[30:33], v[150:153], v[178:181], v[30:33]
	v_mfma_f32_16x16x32_bf16 v[26:29], v[158:161], v[178:181], v[26:29]
	v_mfma_f32_16x16x32_bf16 v[34:37], v[150:153], v[218:221], v[34:37]
	v_mfma_f32_16x16x32_bf16 v[38:41], v[158:161], v[218:221], v[38:41]
	v_mfma_f32_16x16x32_bf16 v[10:13], v[150:153], v[226:229], v[10:13]
	v_mfma_f32_16x16x32_bf16 v[14:17], v[158:161], v[226:229], v[14:17]
	s_setprio 0
	s_barrier
	ds_read_b128 v[130:133], v209
	ds_read_b128 v[134:137], v209 offset:1024
	ds_read_b128 v[138:141], v209 offset:2048
	ds_read_b128 v[142:145], v209 offset:3072
	ds_read_b128 v[146:149], v210
	ds_read_b128 v[150:153], v210 offset:1024
	ds_read_b128 v[154:157], v210 offset:2048
	ds_read_b128 v[158:161], v210 offset:3072
	s_mov_b32 m0, s67
	ds_read_b128 v[162:165], v208 offset:32768
	ds_read_b128 v[166:169], v208 offset:33792
	ds_read_b128 v[170:173], v208 offset:34816
	ds_read_b128 v[178:181], v208 offset:35840
	ds_read_b128 v[214:217], v208 offset:36864
	ds_read_b128 v[218:221], v208 offset:37888
	ds_read_b128 v[222:225], v208 offset:38912
	ds_read_b128 v[226:229], v208 offset:39936
	s_mov_b32 m0, s61
	s_nop 0
	buffer_load_dwordx4 v194, s[68:71], s12 offen lds
	s_mov_b32 m0, s66
	s_nop 0
	buffer_load_dwordx4 v195, s[68:71], s12 offen lds
	s_mov_b32 m0, s67
	s_nop 0
	buffer_load_dwordx4 v196, s[68:71], s12 offen lds
	s_mov_b32 m0, s76
	s_nop 0
	buffer_load_dwordx4 v198, s[68:71], s12 offen lds
	s_waitcnt vmcnt(8)
	s_waitcnt lgkmcnt(0)
	s_barrier
	s_setprio 1
	s_waitcnt lgkmcnt(7)
	v_mfma_f32_16x16x32_bf16 v[126:129], v[130:133], v[162:165], v[126:129]
	v_mfma_f32_16x16x32_bf16 v[122:125], v[138:141], v[162:165], v[122:125]
	s_waitcnt lgkmcnt(5)
	v_mfma_f32_16x16x32_bf16 v[110:113], v[130:133], v[170:173], v[110:113]
	v_mfma_f32_16x16x32_bf16 v[106:109], v[138:141], v[170:173], v[106:109]
	s_waitcnt lgkmcnt(3)
	v_mfma_f32_16x16x32_bf16 v[94:97], v[130:133], v[214:217], v[94:97]
	v_mfma_f32_16x16x32_bf16 v[90:93], v[138:141], v[214:217], v[90:93]
	s_waitcnt lgkmcnt(1)
	v_mfma_f32_16x16x32_bf16 v[78:81], v[130:133], v[222:225], v[78:81]
	v_mfma_f32_16x16x32_bf16 v[74:77], v[138:141], v[222:225], v[74:77]
	v_mfma_f32_16x16x32_bf16 v[126:129], v[134:137], v[166:169], v[126:129]
	v_mfma_f32_16x16x32_bf16 v[122:125], v[142:145], v[166:169], v[122:125]
	v_mfma_f32_16x16x32_bf16 v[110:113], v[134:137], v[178:181], v[110:113]
	v_mfma_f32_16x16x32_bf16 v[106:109], v[142:145], v[178:181], v[106:109]
	v_mfma_f32_16x16x32_bf16 v[94:97], v[134:137], v[218:221], v[94:97]
	v_mfma_f32_16x16x32_bf16 v[90:93], v[142:145], v[218:221], v[90:93]
	s_waitcnt lgkmcnt(0)
	v_mfma_f32_16x16x32_bf16 v[78:81], v[134:137], v[226:229], v[78:81]
	v_mfma_f32_16x16x32_bf16 v[74:77], v[142:145], v[226:229], v[74:77]
	s_setprio 0
	s_setprio 1
	v_mfma_f32_16x16x32_bf16 v[118:121], v[146:149], v[162:165], v[118:121]
	v_mfma_f32_16x16x32_bf16 v[114:117], v[154:157], v[162:165], v[114:117]
	v_mfma_f32_16x16x32_bf16 v[102:105], v[146:149], v[170:173], v[102:105]
	v_mfma_f32_16x16x32_bf16 v[98:101], v[154:157], v[170:173], v[98:101]
	v_mfma_f32_16x16x32_bf16 v[86:89], v[146:149], v[214:217], v[86:89]
	v_mfma_f32_16x16x32_bf16 v[82:85], v[154:157], v[214:217], v[82:85]
	v_mfma_f32_16x16x32_bf16 v[70:73], v[146:149], v[222:225], v[70:73]
	v_mfma_f32_16x16x32_bf16 v[66:69], v[154:157], v[222:225], v[66:69]
	v_mfma_f32_16x16x32_bf16 v[118:121], v[150:153], v[166:169], v[118:121]
	v_mfma_f32_16x16x32_bf16 v[114:117], v[158:161], v[166:169], v[114:117]
	v_mfma_f32_16x16x32_bf16 v[102:105], v[150:153], v[178:181], v[102:105]
	v_mfma_f32_16x16x32_bf16 v[98:101], v[158:161], v[178:181], v[98:101]
	v_mfma_f32_16x16x32_bf16 v[86:89], v[150:153], v[218:221], v[86:89]
	v_mfma_f32_16x16x32_bf16 v[82:85], v[158:161], v[218:221], v[82:85]
	v_mfma_f32_16x16x32_bf16 v[70:73], v[150:153], v[226:229], v[70:73]
	v_mfma_f32_16x16x32_bf16 v[66:69], v[158:161], v[226:229], v[66:69]
	s_setprio 0
	s_barrier
	s_mov_b32 m0, s79
	s_or_b32 s12, s95, 0x80
	ds_read_b128 v[162:165], v208 offset:49152
	ds_read_b128 v[166:169], v208 offset:50176
	ds_read_b128 v[170:173], v208 offset:51200
	ds_read_b128 v[178:181], v208 offset:52224
	ds_read_b128 v[214:217], v208 offset:53248
	ds_read_b128 v[218:221], v208 offset:54272
	ds_read_b128 v[222:225], v208 offset:55296
	ds_read_b128 v[226:229], v208 offset:56320
	buffer_load_dwordx4 v192, s[8:11], s12 offen lds
	s_mov_b32 m0, s80
	s_add_i32 s95, s95, 0x80080
	buffer_load_dwordx4 v193, s[8:11], s12 offen lds
	s_mov_b32 m0, s83
	s_nop 0
	buffer_load_dwordx4 v192, s[8:11], s95 offen lds
	s_mov_b32 m0, s85
	s_nop 0
	buffer_load_dwordx4 v193, s[8:11], s95 offen lds
	s_mov_b32 m0, s81
	s_nop 0
	buffer_load_dwordx4 v194, s[68:71], s59 offen lds
	s_mov_b32 m0, s82
	s_nop 0
	buffer_load_dwordx4 v195, s[68:71], s59 offen lds
	s_waitcnt vmcnt(8)
	s_waitcnt lgkmcnt(0)
	s_barrier
	s_setprio 1
	s_waitcnt lgkmcnt(7)
	v_mfma_f32_16x16x32_bf16 v[62:65], v[130:133], v[162:165], v[62:65]
	v_mfma_f32_16x16x32_bf16 v[58:61], v[138:141], v[162:165], v[58:61]
	s_waitcnt lgkmcnt(5)
	v_mfma_f32_16x16x32_bf16 v[46:49], v[130:133], v[170:173], v[46:49]
	v_mfma_f32_16x16x32_bf16 v[42:45], v[138:141], v[170:173], v[42:45]
	s_waitcnt lgkmcnt(3)
	v_mfma_f32_16x16x32_bf16 v[22:25], v[130:133], v[214:217], v[22:25]
	v_mfma_f32_16x16x32_bf16 v[18:21], v[138:141], v[214:217], v[18:21]
	s_waitcnt lgkmcnt(1)
	v_mfma_f32_16x16x32_bf16 v[6:9], v[130:133], v[222:225], v[6:9]
	v_mfma_f32_16x16x32_bf16 v[2:5], v[138:141], v[222:225], v[2:5]
	v_mfma_f32_16x16x32_bf16 v[62:65], v[134:137], v[166:169], v[62:65]
	v_mfma_f32_16x16x32_bf16 v[58:61], v[142:145], v[166:169], v[58:61]
	v_mfma_f32_16x16x32_bf16 v[46:49], v[134:137], v[178:181], v[46:49]
	v_mfma_f32_16x16x32_bf16 v[42:45], v[142:145], v[178:181], v[42:45]
	v_mfma_f32_16x16x32_bf16 v[22:25], v[134:137], v[218:221], v[22:25]
	v_mfma_f32_16x16x32_bf16 v[18:21], v[142:145], v[218:221], v[18:21]
	s_waitcnt lgkmcnt(0)
	v_mfma_f32_16x16x32_bf16 v[6:9], v[134:137], v[226:229], v[6:9]
	v_mfma_f32_16x16x32_bf16 v[2:5], v[142:145], v[226:229], v[2:5]
	s_setprio 0
	s_setprio 1
	v_mfma_f32_16x16x32_bf16 v[54:57], v[146:149], v[162:165], v[54:57]
	v_mfma_f32_16x16x32_bf16 v[50:53], v[154:157], v[162:165], v[50:53]
	v_mfma_f32_16x16x32_bf16 v[30:33], v[146:149], v[170:173], v[30:33]
	v_mfma_f32_16x16x32_bf16 v[26:29], v[154:157], v[170:173], v[26:29]
	v_mfma_f32_16x16x32_bf16 v[34:37], v[146:149], v[214:217], v[34:37]
	v_mfma_f32_16x16x32_bf16 v[38:41], v[154:157], v[214:217], v[38:41]
	v_mfma_f32_16x16x32_bf16 v[10:13], v[146:149], v[222:225], v[10:13]
	v_mfma_f32_16x16x32_bf16 v[14:17], v[154:157], v[222:225], v[14:17]
	v_mfma_f32_16x16x32_bf16 v[54:57], v[150:153], v[166:169], v[54:57]
	v_mfma_f32_16x16x32_bf16 v[50:53], v[158:161], v[166:169], v[50:53]
	v_mfma_f32_16x16x32_bf16 v[30:33], v[150:153], v[178:181], v[30:33]
	v_mfma_f32_16x16x32_bf16 v[26:29], v[158:161], v[178:181], v[26:29]
	v_mfma_f32_16x16x32_bf16 v[34:37], v[150:153], v[218:221], v[34:37]
	v_mfma_f32_16x16x32_bf16 v[38:41], v[158:161], v[218:221], v[38:41]
	v_mfma_f32_16x16x32_bf16 v[10:13], v[150:153], v[226:229], v[10:13]
	v_mfma_f32_16x16x32_bf16 v[14:17], v[158:161], v[226:229], v[14:17]
	s_setprio 0
	s_barrier
	s_add_i32 s1, s1, 2
	s_addk_i32 vcc_hi, 0x100
	s_addk_i32 s0, 0x100
	s_cmp_gt_u32 s1, 29
	s_cbranch_scc0 .LBB0_115
	s_and_b64 vcc, exec, s[40:41]
	s_cbranch_vccz .LBB0_118
	s_barrier

.LBB0_166:
	ds_read_b128 v[18:21], v175
	ds_read_b128 v[22:25], v175 offset:1024
	ds_read_b128 v[26:29], v175 offset:2048
	ds_read_b128 v[30:33], v175 offset:3072
	ds_read_b128 v[2:5], v176
	ds_read_b128 v[6:9], v176 offset:1024
	ds_read_b128 v[10:13], v176 offset:2048
	ds_read_b128 v[14:17], v176 offset:3072
	s_add_i32 s10, s96, 0x80
	s_cmp_eq_u32 vcc_lo, 12
	s_cselect_b32 s13, s92, s10
	s_cselect_b32 s12, s93, s97
	s_or_b32 vcc_hi, s13, 0x80
	s_mov_b32 m0, s79
	ds_read_b128 v[180:183], v177
	ds_read_b128 v[184:187], v177 offset:1024
	ds_read_b128 v[188:191], v177 offset:2048
	ds_read_b128 v[192:195], v177 offset:3072
	ds_read_b128 v[198:201], v177 offset:4096
	ds_read_b128 v[202:205], v177 offset:5120
	ds_read_b128 v[206:209], v177 offset:6144
	ds_read_b128 v[210:213], v177 offset:7168
	buffer_load_dwordx4 v172, s[4:7], s96 offen lds
	s_mov_b32 m0, s80
	s_nop 0
	buffer_load_dwordx4 v173, s[4:7], s96 offen lds
	s_waitcnt vmcnt(8)
	s_waitcnt lgkmcnt(0)
	s_barrier
	s_setprio 1
	s_waitcnt lgkmcnt(6)
	v_mfma_f32_16x16x128_f8f6f4 v[158:161], v[18:25], v[180:187], v[158:161]
	v_mfma_f32_16x16x128_f8f6f4 v[154:157], v[26:33], v[180:187], v[154:157]
	s_waitcnt lgkmcnt(4)
	v_mfma_f32_16x16x128_f8f6f4 v[150:153], v[18:25], v[188:195], v[150:153]
	v_mfma_f32_16x16x128_f8f6f4 v[142:145], v[26:33], v[188:195], v[142:145]
	s_waitcnt lgkmcnt(2)
	v_mfma_f32_16x16x128_f8f6f4 v[134:137], v[18:25], v[198:205], v[134:137]
	v_mfma_f32_16x16x128_f8f6f4 v[126:129], v[26:33], v[198:205], v[126:129]
	s_waitcnt lgkmcnt(0)
	v_mfma_f32_16x16x128_f8f6f4 v[118:121], v[18:25], v[206:213], v[118:121]
	v_mfma_f32_16x16x128_f8f6f4 v[110:113], v[26:33], v[206:213], v[110:113]
	s_setprio 0
	s_setprio 1
	v_mfma_f32_16x16x128_f8f6f4 v[146:149], v[2:9], v[180:187], v[146:149]
	v_mfma_f32_16x16x128_f8f6f4 v[138:141], v[10:17], v[180:187], v[138:141]
	v_mfma_f32_16x16x128_f8f6f4 v[130:133], v[2:9], v[188:195], v[130:133]
	v_mfma_f32_16x16x128_f8f6f4 v[122:125], v[10:17], v[188:195], v[122:125]
	v_mfma_f32_16x16x128_f8f6f4 v[114:117], v[2:9], v[198:205], v[114:117]
	v_mfma_f32_16x16x128_f8f6f4 v[106:109], v[10:17], v[198:205], v[106:109]
	v_mfma_f32_16x16x128_f8f6f4 v[102:105], v[2:9], v[206:213], v[102:105]
	v_mfma_f32_16x16x128_f8f6f4 v[98:101], v[10:17], v[206:213], v[98:101]
	s_setprio 0
	s_barrier
	s_mov_b32 m0, s59
	s_mov_b32 s10, s6
	s_mov_b32 s11, s7
	ds_read_b128 v[180:183], v177 offset:16384
	ds_read_b128 v[184:187], v177 offset:17408
	ds_read_b128 v[188:191], v177 offset:18432
	ds_read_b128 v[192:195], v177 offset:19456
	ds_read_b128 v[198:201], v177 offset:20480
	ds_read_b128 v[202:205], v177 offset:21504
	ds_read_b128 v[206:209], v177 offset:22528
	ds_read_b128 v[210:213], v177 offset:23552
	buffer_load_dwordx4 v168, s[8:11], s12 offen lds
	s_mov_b32 m0, s60
	s_add_i32 s95, s12, 0x40000
	buffer_load_dwordx4 v169, s[8:11], s12 offen lds
	s_mov_b32 m0, s61
	s_nop 0
	buffer_load_dwordx4 v168, s[8:11], s95 offen lds
	s_mov_b32 m0, s62
	s_nop 0
	buffer_load_dwordx4 v169, s[8:11], s95 offen lds
	s_waitcnt vmcnt(6)
	s_waitcnt lgkmcnt(0)
	s_barrier
	s_setprio 1
	s_waitcnt lgkmcnt(6)
	v_mfma_f32_16x16x128_f8f6f4 v[94:97], v[18:25], v[180:187], v[94:97]
	v_mfma_f32_16x16x128_f8f6f4 v[90:93], v[26:33], v[180:187], v[90:93]
	s_waitcnt lgkmcnt(4)
	v_mfma_f32_16x16x128_f8f6f4 v[78:81], v[18:25], v[188:195], v[78:81]
	v_mfma_f32_16x16x128_f8f6f4 v[62:65], v[26:33], v[188:195], v[62:65]
	s_waitcnt lgkmcnt(2)
	v_mfma_f32_16x16x128_f8f6f4 v[54:57], v[18:25], v[198:205], v[54:57]
	v_mfma_f32_16x16x128_f8f6f4 v[46:49], v[26:33], v[198:205], v[46:49]
	s_waitcnt lgkmcnt(0)
	v_mfma_f32_16x16x128_f8f6f4 v[38:41], v[18:25], v[206:213], v[38:41]
	v_mfma_f32_16x16x128_f8f6f4 v[34:37], v[26:33], v[206:213], v[34:37]
	s_setprio 0
	s_setprio 1
	v_mfma_f32_16x16x128_f8f6f4 v[74:77], v[2:9], v[180:187], v[74:77]
	v_mfma_f32_16x16x128_f8f6f4 v[58:61], v[10:17], v[180:187], v[58:61]
	v_mfma_f32_16x16x128_f8f6f4 v[50:53], v[2:9], v[188:195], v[50:53]
	v_mfma_f32_16x16x128_f8f6f4 v[42:45], v[10:17], v[188:195], v[42:45]
	v_mfma_f32_16x16x128_f8f6f4 v[86:89], v[2:9], v[198:205], v[86:89]
	v_mfma_f32_16x16x128_f8f6f4 v[82:85], v[10:17], v[198:205], v[82:85]
	v_mfma_f32_16x16x128_f8f6f4 v[70:73], v[2:9], v[206:213], v[70:73]
	v_mfma_f32_16x16x128_f8f6f4 v[66:69], v[10:17], v[206:213], v[66:69]
	s_setprio 0
	s_barrier
	ds_read_b128 v[2:5], v178
	ds_read_b128 v[6:9], v178 offset:1024
	ds_read_b128 v[10:13], v178 offset:2048
	ds_read_b128 v[14:17], v178 offset:3072
	ds_read_b128 v[18:21], v179
	ds_read_b128 v[22:25], v179 offset:1024
	ds_read_b128 v[26:29], v179 offset:2048
	ds_read_b128 v[30:33], v179 offset:3072
	s_mov_b32 m0, s64
	ds_read_b128 v[180:183], v177 offset:32768
	ds_read_b128 v[184:187], v177 offset:33792
	ds_read_b128 v[188:191], v177 offset:34816
	ds_read_b128 v[192:195], v177 offset:35840
	ds_read_b128 v[198:201], v177 offset:36864
	ds_read_b128 v[202:205], v177 offset:37888
	ds_read_b128 v[206:209], v177 offset:38912
	ds_read_b128 v[210:213], v177 offset:39936
	s_mov_b32 m0, s58
	s_nop 0
	buffer_load_dwordx4 v170, s[4:7], s13 offen lds
	s_mov_b32 m0, s63
	s_nop 0
	buffer_load_dwordx4 v171, s[4:7], s13 offen lds
	s_mov_b32 m0, s64
	s_nop 0
	buffer_load_dwordx4 v172, s[4:7], s13 offen lds
	s_mov_b32 m0, s65
	s_nop 0
	buffer_load_dwordx4 v173, s[4:7], s13 offen lds
	s_waitcnt vmcnt(8)
	s_waitcnt lgkmcnt(0)
	s_barrier
	s_setprio 1
	s_waitcnt lgkmcnt(6)
	v_mfma_f32_16x16x128_f8f6f4 v[158:161], v[2:9], v[180:187], v[158:161]
	v_mfma_f32_16x16x128_f8f6f4 v[154:157], v[10:17], v[180:187], v[154:157]
	s_waitcnt lgkmcnt(4)
	v_mfma_f32_16x16x128_f8f6f4 v[150:153], v[2:9], v[188:195], v[150:153]
	v_mfma_f32_16x16x128_f8f6f4 v[142:145], v[10:17], v[188:195], v[142:145]
	s_waitcnt lgkmcnt(2)
	v_mfma_f32_16x16x128_f8f6f4 v[134:137], v[2:9], v[198:205], v[134:137]
	v_mfma_f32_16x16x128_f8f6f4 v[126:129], v[10:17], v[198:205], v[126:129]
	s_waitcnt lgkmcnt(0)
	v_mfma_f32_16x16x128_f8f6f4 v[118:121], v[2:9], v[206:213], v[118:121]
	v_mfma_f32_16x16x128_f8f6f4 v[110:113], v[10:17], v[206:213], v[110:113]
	s_setprio 0
	s_setprio 1
	v_mfma_f32_16x16x128_f8f6f4 v[146:149], v[18:25], v[180:187], v[146:149]
	v_mfma_f32_16x16x128_f8f6f4 v[138:141], v[26:33], v[180:187], v[138:141]
	v_mfma_f32_16x16x128_f8f6f4 v[130:133], v[18:25], v[188:195], v[130:133]
	v_mfma_f32_16x16x128_f8f6f4 v[122:125], v[26:33], v[188:195], v[122:125]
	v_mfma_f32_16x16x128_f8f6f4 v[114:117], v[18:25], v[198:205], v[114:117]
	v_mfma_f32_16x16x128_f8f6f4 v[106:109], v[26:33], v[198:205], v[106:109]
	v_mfma_f32_16x16x128_f8f6f4 v[102:105], v[18:25], v[206:213], v[102:105]
	v_mfma_f32_16x16x128_f8f6f4 v[98:101], v[26:33], v[206:213], v[98:101]
	s_setprio 0
	s_barrier
	s_mov_b32 m0, s67
	s_or_b32 s13, s12, 0x80
	ds_read_b128 v[180:183], v177 offset:49152
	ds_read_b128 v[184:187], v177 offset:50176
	ds_read_b128 v[188:191], v177 offset:51200
	ds_read_b128 v[192:195], v177 offset:52224
	ds_read_b128 v[198:201], v177 offset:53248
	ds_read_b128 v[202:205], v177 offset:54272
	ds_read_b128 v[206:209], v177 offset:55296
	ds_read_b128 v[210:213], v177 offset:56320
	buffer_load_dwordx4 v168, s[8:11], s13 offen lds
	s_mov_b32 m0, s69
	s_add_i32 s12, s12, 0x40080
	buffer_load_dwordx4 v169, s[8:11], s13 offen lds
	s_mov_b32 m0, s76
	s_nop 0
	buffer_load_dwordx4 v168, s[8:11], s12 offen lds
	s_mov_b32 m0, s77
	s_nop 0
	buffer_load_dwordx4 v169, s[8:11], s12 offen lds
	s_mov_b32 m0, s70
	s_nop 0
	buffer_load_dwordx4 v170, s[4:7], vcc_hi offen lds
	s_mov_b32 m0, s71
	s_nop 0
	buffer_load_dwordx4 v171, s[4:7], vcc_hi offen lds
	s_waitcnt vmcnt(8)
	s_waitcnt lgkmcnt(0)
	s_barrier
	s_setprio 1
	s_waitcnt lgkmcnt(6)
	v_mfma_f32_16x16x128_f8f6f4 v[94:97], v[2:9], v[180:187], v[94:97]
	v_mfma_f32_16x16x128_f8f6f4 v[90:93], v[10:17], v[180:187], v[90:93]
	s_waitcnt lgkmcnt(4)
	v_mfma_f32_16x16x128_f8f6f4 v[78:81], v[2:9], v[188:195], v[78:81]
	v_mfma_f32_16x16x128_f8f6f4 v[62:65], v[10:17], v[188:195], v[62:65]
	s_waitcnt lgkmcnt(2)
	v_mfma_f32_16x16x128_f8f6f4 v[54:57], v[2:9], v[198:205], v[54:57]
	v_mfma_f32_16x16x128_f8f6f4 v[46:49], v[10:17], v[198:205], v[46:49]
	s_waitcnt lgkmcnt(0)
	v_mfma_f32_16x16x128_f8f6f4 v[38:41], v[2:9], v[206:213], v[38:41]
	v_mfma_f32_16x16x128_f8f6f4 v[34:37], v[10:17], v[206:213], v[34:37]
	s_setprio 0
	s_setprio 1
	v_mfma_f32_16x16x128_f8f6f4 v[74:77], v[18:25], v[180:187], v[74:77]
	v_mfma_f32_16x16x128_f8f6f4 v[58:61], v[26:33], v[180:187], v[58:61]
	v_mfma_f32_16x16x128_f8f6f4 v[50:53], v[18:25], v[188:195], v[50:53]
	v_mfma_f32_16x16x128_f8f6f4 v[42:45], v[26:33], v[188:195], v[42:45]
	v_mfma_f32_16x16x128_f8f6f4 v[86:89], v[18:25], v[198:205], v[86:89]
	v_mfma_f32_16x16x128_f8f6f4 v[82:85], v[26:33], v[198:205], v[82:85]
	v_mfma_f32_16x16x128_f8f6f4 v[70:73], v[18:25], v[206:213], v[70:73]
	v_mfma_f32_16x16x128_f8f6f4 v[66:69], v[26:33], v[206:213], v[66:69]
	s_setprio 0
	s_barrier
	s_add_i32 vcc_lo, vcc_lo, 2
	s_addk_i32 s96, 0x100
	s_addk_i32 s97, 0x100
	s_cmp_gt_u32 vcc_lo, 13
	s_cbranch_scc0 .LBB0_166
	s_nop 15
	s_nop 15
	s_and_b64 vcc, exec, s[16:17]
	s_cbranch_vccz .LBB0_169
	s_barrier

.LBB0_522:
	ds_read_b128 v[134:137], v147
	ds_read_b128 v[152:155], v147 offset:1024
	ds_read_b128 v[156:159], v147 offset:2048
	ds_read_b128 v[160:163], v147 offset:3072
	ds_read_b128 v[164:167], v148
	ds_read_b128 v[168:171], v148 offset:1024
	ds_read_b128 v[172:175], v148 offset:2048
	ds_read_b128 v[176:179], v148 offset:3072
	s_add_i32 s46, s76, 0x80
	s_cmp_eq_u32 s78, 28
	s_cselect_b32 s81, s73, s46
	s_cselect_b32 s80, s75, s77
	s_or_b32 s79, s81, 0x80
	s_mov_b32 m0, s65
	ds_read_b128 v[180:183], v149
	ds_read_b128 v[184:187], v149 offset:1024
	ds_read_b128 v[188:191], v149 offset:2048
	ds_read_b128 v[192:195], v149 offset:3072
	ds_read_b128 v[198:201], v149 offset:4096
	ds_read_b128 v[202:205], v149 offset:5120
	ds_read_b128 v[206:209], v149 offset:6144
	ds_read_b128 v[210:213], v149 offset:7168
	buffer_load_dwordx4 v143, s[8:11], s76 offen lds
	s_mov_b32 m0, s66
	s_nop 0
	buffer_load_dwordx4 v144, s[8:11], s76 offen lds
	s_waitcnt vmcnt(8)
	s_waitcnt lgkmcnt(0)
	s_barrier
	s_setprio 1
	s_waitcnt lgkmcnt(7)
	v_mfma_f32_16x16x32_bf16 v[126:129], v[134:137], v[180:183], v[126:129]
	v_mfma_f32_16x16x32_bf16 v[122:125], v[156:159], v[180:183], v[122:125]
	s_waitcnt lgkmcnt(5)
	v_mfma_f32_16x16x32_bf16 v[110:113], v[134:137], v[188:191], v[110:113]
	v_mfma_f32_16x16x32_bf16 v[106:109], v[156:159], v[188:191], v[106:109]
	s_waitcnt lgkmcnt(3)
	v_mfma_f32_16x16x32_bf16 v[94:97], v[134:137], v[198:201], v[94:97]
	v_mfma_f32_16x16x32_bf16 v[90:93], v[156:159], v[198:201], v[90:93]
	s_waitcnt lgkmcnt(1)
	v_mfma_f32_16x16x32_bf16 v[78:81], v[134:137], v[206:209], v[78:81]
	v_mfma_f32_16x16x32_bf16 v[74:77], v[156:159], v[206:209], v[74:77]
	v_mfma_f32_16x16x32_bf16 v[126:129], v[152:155], v[184:187], v[126:129]
	v_mfma_f32_16x16x32_bf16 v[122:125], v[160:163], v[184:187], v[122:125]
	v_mfma_f32_16x16x32_bf16 v[110:113], v[152:155], v[192:195], v[110:113]
	v_mfma_f32_16x16x32_bf16 v[106:109], v[160:163], v[192:195], v[106:109]
	v_mfma_f32_16x16x32_bf16 v[94:97], v[152:155], v[202:205], v[94:97]
	v_mfma_f32_16x16x32_bf16 v[90:93], v[160:163], v[202:205], v[90:93]
	s_waitcnt lgkmcnt(0)
	v_mfma_f32_16x16x32_bf16 v[78:81], v[152:155], v[210:213], v[78:81]
	v_mfma_f32_16x16x32_bf16 v[74:77], v[160:163], v[210:213], v[74:77]
	s_setprio 0
	s_setprio 1
	v_mfma_f32_16x16x32_bf16 v[118:121], v[164:167], v[180:183], v[118:121]
	v_mfma_f32_16x16x32_bf16 v[114:117], v[172:175], v[180:183], v[114:117]
	v_mfma_f32_16x16x32_bf16 v[102:105], v[164:167], v[188:191], v[102:105]
	v_mfma_f32_16x16x32_bf16 v[98:101], v[172:175], v[188:191], v[98:101]
	v_mfma_f32_16x16x32_bf16 v[86:89], v[164:167], v[198:201], v[86:89]
	v_mfma_f32_16x16x32_bf16 v[82:85], v[172:175], v[198:201], v[82:85]
	v_mfma_f32_16x16x32_bf16 v[70:73], v[164:167], v[206:209], v[70:73]
	v_mfma_f32_16x16x32_bf16 v[66:69], v[172:175], v[206:209], v[66:69]
	v_mfma_f32_16x16x32_bf16 v[118:121], v[168:171], v[184:187], v[118:121]
	v_mfma_f32_16x16x32_bf16 v[114:117], v[176:179], v[184:187], v[114:117]
	v_mfma_f32_16x16x32_bf16 v[102:105], v[168:171], v[192:195], v[102:105]
	v_mfma_f32_16x16x32_bf16 v[98:101], v[176:179], v[192:195], v[98:101]
	v_mfma_f32_16x16x32_bf16 v[86:89], v[168:171], v[202:205], v[86:89]
	v_mfma_f32_16x16x32_bf16 v[82:85], v[176:179], v[202:205], v[82:85]
	v_mfma_f32_16x16x32_bf16 v[70:73], v[168:171], v[210:213], v[70:73]
	v_mfma_f32_16x16x32_bf16 v[66:69], v[176:179], v[210:213], v[66:69]
	s_setprio 0
	s_barrier
	s_mov_b32 m0, s49
	s_mov_b32 s46, s10
	s_mov_b32 s47, s11
	ds_read_b128 v[180:183], v149 offset:16384
	ds_read_b128 v[184:187], v149 offset:17408
	ds_read_b128 v[188:191], v149 offset:18432
	ds_read_b128 v[192:195], v149 offset:19456
	ds_read_b128 v[198:201], v149 offset:20480
	ds_read_b128 v[202:205], v149 offset:21504
	ds_read_b128 v[206:209], v149 offset:22528
	ds_read_b128 v[210:213], v149 offset:23552
	buffer_load_dwordx4 v1, s[44:47], s80 offen lds
	s_mov_b32 m0, s52
	s_add_i32 s82, s80, 0x80000
	buffer_load_dwordx4 v140, s[44:47], s80 offen lds
	s_mov_b32 m0, s53
	s_nop 0
	buffer_load_dwordx4 v1, s[44:47], s82 offen lds
	s_mov_b32 m0, s54
	s_nop 0
	buffer_load_dwordx4 v140, s[44:47], s82 offen lds
	s_waitcnt vmcnt(6)
	s_waitcnt lgkmcnt(0)
	s_barrier
	s_setprio 1
	s_waitcnt lgkmcnt(7)
	v_mfma_f32_16x16x32_bf16 v[62:65], v[134:137], v[180:183], v[62:65]
	v_mfma_f32_16x16x32_bf16 v[58:61], v[156:159], v[180:183], v[58:61]
	s_waitcnt lgkmcnt(5)
	v_mfma_f32_16x16x32_bf16 v[46:49], v[134:137], v[188:191], v[46:49]
	v_mfma_f32_16x16x32_bf16 v[42:45], v[156:159], v[188:191], v[42:45]
	s_waitcnt lgkmcnt(3)
	v_mfma_f32_16x16x32_bf16 v[22:25], v[134:137], v[198:201], v[22:25]
	v_mfma_f32_16x16x32_bf16 v[18:21], v[156:159], v[198:201], v[18:21]
	s_waitcnt lgkmcnt(1)
	v_mfma_f32_16x16x32_bf16 v[6:9], v[134:137], v[206:209], v[6:9]
	v_mfma_f32_16x16x32_bf16 v[2:5], v[156:159], v[206:209], v[2:5]
	v_mfma_f32_16x16x32_bf16 v[62:65], v[152:155], v[184:187], v[62:65]
	v_mfma_f32_16x16x32_bf16 v[58:61], v[160:163], v[184:187], v[58:61]
	v_mfma_f32_16x16x32_bf16 v[46:49], v[152:155], v[192:195], v[46:49]
	v_mfma_f32_16x16x32_bf16 v[42:45], v[160:163], v[192:195], v[42:45]
	v_mfma_f32_16x16x32_bf16 v[22:25], v[152:155], v[202:205], v[22:25]
	v_mfma_f32_16x16x32_bf16 v[18:21], v[160:163], v[202:205], v[18:21]
	s_waitcnt lgkmcnt(0)
	v_mfma_f32_16x16x32_bf16 v[6:9], v[152:155], v[210:213], v[6:9]
	v_mfma_f32_16x16x32_bf16 v[2:5], v[160:163], v[210:213], v[2:5]
	s_setprio 0
	s_setprio 1
	v_mfma_f32_16x16x32_bf16 v[54:57], v[164:167], v[180:183], v[54:57]
	v_mfma_f32_16x16x32_bf16 v[50:53], v[172:175], v[180:183], v[50:53]
	v_mfma_f32_16x16x32_bf16 v[30:33], v[164:167], v[188:191], v[30:33]
	v_mfma_f32_16x16x32_bf16 v[26:29], v[172:175], v[188:191], v[26:29]
	v_mfma_f32_16x16x32_bf16 v[34:37], v[164:167], v[198:201], v[34:37]
	v_mfma_f32_16x16x32_bf16 v[38:41], v[172:175], v[198:201], v[38:41]
	v_mfma_f32_16x16x32_bf16 v[10:13], v[164:167], v[206:209], v[10:13]
	v_mfma_f32_16x16x32_bf16 v[14:17], v[172:175], v[206:209], v[14:17]
	v_mfma_f32_16x16x32_bf16 v[54:57], v[168:171], v[184:187], v[54:57]
	v_mfma_f32_16x16x32_bf16 v[50:53], v[176:179], v[184:187], v[50:53]
	v_mfma_f32_16x16x32_bf16 v[30:33], v[168:171], v[192:195], v[30:33]
	v_mfma_f32_16x16x32_bf16 v[26:29], v[176:179], v[192:195], v[26:29]
	v_mfma_f32_16x16x32_bf16 v[34:37], v[168:171], v[202:205], v[34:37]
	v_mfma_f32_16x16x32_bf16 v[38:41], v[176:179], v[202:205], v[38:41]
	v_mfma_f32_16x16x32_bf16 v[10:13], v[168:171], v[210:213], v[10:13]
	v_mfma_f32_16x16x32_bf16 v[14:17], v[176:179], v[210:213], v[14:17]
	s_setprio 0
	s_barrier
	ds_read_b128 v[134:137], v150
	ds_read_b128 v[152:155], v150 offset:1024
	ds_read_b128 v[156:159], v150 offset:2048
	ds_read_b128 v[160:163], v150 offset:3072
	ds_read_b128 v[164:167], v151
	ds_read_b128 v[168:171], v151 offset:1024
	ds_read_b128 v[172:175], v151 offset:2048
	ds_read_b128 v[176:179], v151 offset:3072
	s_mov_b32 m0, s56
	ds_read_b128 v[180:183], v149 offset:32768
	ds_read_b128 v[184:187], v149 offset:33792
	ds_read_b128 v[188:191], v149 offset:34816
	ds_read_b128 v[192:195], v149 offset:35840
	ds_read_b128 v[198:201], v149 offset:36864
	ds_read_b128 v[202:205], v149 offset:37888
	ds_read_b128 v[206:209], v149 offset:38912
	ds_read_b128 v[210:213], v149 offset:39936
	s_mov_b32 m0, s48
	s_nop 0
	buffer_load_dwordx4 v141, s[8:11], s81 offen lds
	s_mov_b32 m0, s55
	s_nop 0
	buffer_load_dwordx4 v142, s[8:11], s81 offen lds
	s_mov_b32 m0, s56
	s_nop 0
	buffer_load_dwordx4 v143, s[8:11], s81 offen lds
	s_mov_b32 m0, s57
	s_nop 0
	buffer_load_dwordx4 v144, s[8:11], s81 offen lds
	s_waitcnt vmcnt(8)
	s_waitcnt lgkmcnt(0)
	s_barrier
	s_setprio 1
	s_waitcnt lgkmcnt(7)
	v_mfma_f32_16x16x32_bf16 v[126:129], v[134:137], v[180:183], v[126:129]
	v_mfma_f32_16x16x32_bf16 v[122:125], v[156:159], v[180:183], v[122:125]
	s_waitcnt lgkmcnt(5)
	v_mfma_f32_16x16x32_bf16 v[110:113], v[134:137], v[188:191], v[110:113]
	v_mfma_f32_16x16x32_bf16 v[106:109], v[156:159], v[188:191], v[106:109]
	s_waitcnt lgkmcnt(3)
	v_mfma_f32_16x16x32_bf16 v[94:97], v[134:137], v[198:201], v[94:97]
	v_mfma_f32_16x16x32_bf16 v[90:93], v[156:159], v[198:201], v[90:93]
	s_waitcnt lgkmcnt(1)
	v_mfma_f32_16x16x32_bf16 v[78:81], v[134:137], v[206:209], v[78:81]
	v_mfma_f32_16x16x32_bf16 v[74:77], v[156:159], v[206:209], v[74:77]
	v_mfma_f32_16x16x32_bf16 v[126:129], v[152:155], v[184:187], v[126:129]
	v_mfma_f32_16x16x32_bf16 v[122:125], v[160:163], v[184:187], v[122:125]
	v_mfma_f32_16x16x32_bf16 v[110:113], v[152:155], v[192:195], v[110:113]
	v_mfma_f32_16x16x32_bf16 v[106:109], v[160:163], v[192:195], v[106:109]
	v_mfma_f32_16x16x32_bf16 v[94:97], v[152:155], v[202:205], v[94:97]
	v_mfma_f32_16x16x32_bf16 v[90:93], v[160:163], v[202:205], v[90:93]
	s_waitcnt lgkmcnt(0)
	v_mfma_f32_16x16x32_bf16 v[78:81], v[152:155], v[210:213], v[78:81]
	v_mfma_f32_16x16x32_bf16 v[74:77], v[160:163], v[210:213], v[74:77]
	s_setprio 0
	s_setprio 1
	v_mfma_f32_16x16x32_bf16 v[118:121], v[164:167], v[180:183], v[118:121]
	v_mfma_f32_16x16x32_bf16 v[114:117], v[172:175], v[180:183], v[114:117]
	v_mfma_f32_16x16x32_bf16 v[102:105], v[164:167], v[188:191], v[102:105]
	v_mfma_f32_16x16x32_bf16 v[98:101], v[172:175], v[188:191], v[98:101]
	v_mfma_f32_16x16x32_bf16 v[86:89], v[164:167], v[198:201], v[86:89]
	v_mfma_f32_16x16x32_bf16 v[82:85], v[172:175], v[198:201], v[82:85]
	v_mfma_f32_16x16x32_bf16 v[70:73], v[164:167], v[206:209], v[70:73]
	v_mfma_f32_16x16x32_bf16 v[66:69], v[172:175], v[206:209], v[66:69]
	v_mfma_f32_16x16x32_bf16 v[118:121], v[168:171], v[184:187], v[118:121]
	v_mfma_f32_16x16x32_bf16 v[114:117], v[176:179], v[184:187], v[114:117]
	v_mfma_f32_16x16x32_bf16 v[102:105], v[168:171], v[192:195], v[102:105]
	v_mfma_f32_16x16x32_bf16 v[98:101], v[176:179], v[192:195], v[98:101]
	v_mfma_f32_16x16x32_bf16 v[86:89], v[168:171], v[202:205], v[86:89]
	v_mfma_f32_16x16x32_bf16 v[82:85], v[176:179], v[202:205], v[82:85]
	v_mfma_f32_16x16x32_bf16 v[70:73], v[168:171], v[210:213], v[70:73]
	v_mfma_f32_16x16x32_bf16 v[66:69], v[176:179], v[210:213], v[66:69]
	s_setprio 0
	s_barrier
	s_mov_b32 m0, s58
	s_or_b32 s81, s80, 0x80
	ds_read_b128 v[180:183], v149 offset:49152
	ds_read_b128 v[184:187], v149 offset:50176
	ds_read_b128 v[188:191], v149 offset:51200
	ds_read_b128 v[192:195], v149 offset:52224
	ds_read_b128 v[198:201], v149 offset:53248
	ds_read_b128 v[202:205], v149 offset:54272
	ds_read_b128 v[206:209], v149 offset:55296
	ds_read_b128 v[210:213], v149 offset:56320
	buffer_load_dwordx4 v1, s[44:47], s81 offen lds
	s_mov_b32 m0, s59
	s_add_i32 s80, s80, 0x80080
	buffer_load_dwordx4 v140, s[44:47], s81 offen lds
	s_mov_b32 m0, s62
	s_nop 0
	buffer_load_dwordx4 v1, s[44:47], s80 offen lds
	s_mov_b32 m0, s63
	s_nop 0
	buffer_load_dwordx4 v140, s[44:47], s80 offen lds
	s_mov_b32 m0, s60
	s_nop 0
	buffer_load_dwordx4 v141, s[8:11], s79 offen lds
	s_mov_b32 m0, s61
	s_nop 0
	buffer_load_dwordx4 v142, s[8:11], s79 offen lds
	s_waitcnt vmcnt(8)
	s_waitcnt lgkmcnt(0)
	s_barrier
	s_setprio 1
	s_waitcnt lgkmcnt(7)
	v_mfma_f32_16x16x32_bf16 v[62:65], v[134:137], v[180:183], v[62:65]
	v_mfma_f32_16x16x32_bf16 v[58:61], v[156:159], v[180:183], v[58:61]
	s_waitcnt lgkmcnt(5)
	v_mfma_f32_16x16x32_bf16 v[46:49], v[134:137], v[188:191], v[46:49]
	v_mfma_f32_16x16x32_bf16 v[42:45], v[156:159], v[188:191], v[42:45]
	s_waitcnt lgkmcnt(3)
	v_mfma_f32_16x16x32_bf16 v[22:25], v[134:137], v[198:201], v[22:25]
	v_mfma_f32_16x16x32_bf16 v[18:21], v[156:159], v[198:201], v[18:21]
	s_waitcnt lgkmcnt(1)
	v_mfma_f32_16x16x32_bf16 v[6:9], v[134:137], v[206:209], v[6:9]
	v_mfma_f32_16x16x32_bf16 v[2:5], v[156:159], v[206:209], v[2:5]
	v_mfma_f32_16x16x32_bf16 v[62:65], v[152:155], v[184:187], v[62:65]
	v_mfma_f32_16x16x32_bf16 v[58:61], v[160:163], v[184:187], v[58:61]
	v_mfma_f32_16x16x32_bf16 v[46:49], v[152:155], v[192:195], v[46:49]
	v_mfma_f32_16x16x32_bf16 v[42:45], v[160:163], v[192:195], v[42:45]
	v_mfma_f32_16x16x32_bf16 v[22:25], v[152:155], v[202:205], v[22:25]
	v_mfma_f32_16x16x32_bf16 v[18:21], v[160:163], v[202:205], v[18:21]
	s_waitcnt lgkmcnt(0)
	v_mfma_f32_16x16x32_bf16 v[6:9], v[152:155], v[210:213], v[6:9]
	v_mfma_f32_16x16x32_bf16 v[2:5], v[160:163], v[210:213], v[2:5]
	s_setprio 0
	s_setprio 1
	v_mfma_f32_16x16x32_bf16 v[54:57], v[164:167], v[180:183], v[54:57]
	v_mfma_f32_16x16x32_bf16 v[50:53], v[172:175], v[180:183], v[50:53]
	v_mfma_f32_16x16x32_bf16 v[30:33], v[164:167], v[188:191], v[30:33]
	v_mfma_f32_16x16x32_bf16 v[26:29], v[172:175], v[188:191], v[26:29]
	v_mfma_f32_16x16x32_bf16 v[34:37], v[164:167], v[198:201], v[34:37]
	v_mfma_f32_16x16x32_bf16 v[38:41], v[172:175], v[198:201], v[38:41]
	v_mfma_f32_16x16x32_bf16 v[10:13], v[164:167], v[206:209], v[10:13]
	v_mfma_f32_16x16x32_bf16 v[14:17], v[172:175], v[206:209], v[14:17]
	v_mfma_f32_16x16x32_bf16 v[54:57], v[168:171], v[184:187], v[54:57]
	v_mfma_f32_16x16x32_bf16 v[50:53], v[176:179], v[184:187], v[50:53]
	v_mfma_f32_16x16x32_bf16 v[30:33], v[168:171], v[192:195], v[30:33]
	v_mfma_f32_16x16x32_bf16 v[26:29], v[176:179], v[192:195], v[26:29]
	v_mfma_f32_16x16x32_bf16 v[34:37], v[168:171], v[202:205], v[34:37]
	v_mfma_f32_16x16x32_bf16 v[38:41], v[176:179], v[202:205], v[38:41]
	v_mfma_f32_16x16x32_bf16 v[10:13], v[168:171], v[210:213], v[10:13]
	v_mfma_f32_16x16x32_bf16 v[14:17], v[176:179], v[210:213], v[14:17]
	s_setprio 0
	s_barrier
	s_add_i32 s78, s78, 2
	s_addk_i32 s76, 0x100
	s_addk_i32 s77, 0x100
	s_cmp_gt_u32 s78, 29
	s_cbranch_scc0 .LBB0_522
	s_and_b64 vcc, exec, s[6:7]
	s_cbranch_vccz .LBB0_525
	s_barrier

.LBB0_1072:
	v_add_u32_e32 v0, 0x10000, v181
	ds_read_b128 v[18:21], v0
	ds_read_b128 v[22:25], v0 offset:1024
	ds_read_b128 v[26:29], v0 offset:2048
	ds_read_b128 v[30:33], v0 offset:3072
	v_add_u32_e32 v0, 0x14000, v181
	ds_read_b128 v[2:5], v0
	ds_read_b128 v[6:9], v0 offset:1024
	ds_read_b128 v[10:13], v0 offset:2048
	ds_read_b128 v[14:17], v0 offset:3072
	s_add_i32 vcc_hi, s94, 0xffffff80
	s_and_b64 s[42:43], s[0:1], exec
	s_cselect_b32 vcc_lo, 0, s94
	s_add_i32 s95, s91, s94
	s_and_b64 s[42:43], s[0:1], exec
	s_cselect_b32 s96, s53, s95
	s_or_b32 s95, vcc_lo, 0x80
	s_or_b32 s97, s96, 0x80
	v_cndmask_b32_e64 v192, v186, v178, s[0:1]
	v_cndmask_b32_e64 v191, v187, v180, s[0:1]
	v_cndmask_b32_e64 v0, v188, v182, s[0:1]
	v_cndmask_b32_e64 v193, v189, v184, s[0:1]
	s_mov_b32 m0, s80
	ds_read_b128 v[198:201], v183
	ds_read_b128 v[202:205], v183 offset:1024
	ds_read_b128 v[206:209], v183 offset:2048
	ds_read_b128 v[210:213], v183 offset:3072
	ds_read_b128 v[214:217], v183 offset:4096
	ds_read_b128 v[218:221], v183 offset:5120
	ds_read_b128 v[222:225], v183 offset:6144
	ds_read_b128 v[226:229], v183 offset:7168
	buffer_load_dwordx4 v188, s[68:71], vcc_hi offen lds
	s_mov_b32 m0, s81
	s_nop 0
	buffer_load_dwordx4 v189, s[68:71], vcc_hi offen lds
	s_waitcnt vmcnt(8)
	s_waitcnt lgkmcnt(0)
	s_barrier
	s_setprio 1
	s_waitcnt lgkmcnt(0)
	v_mfma_f32_16x16x128_f8f6f4 v[158:161], v[18:25], v[198:205], v[158:161]
	v_mfma_f32_16x16x128_f8f6f4 v[154:157], v[26:33], v[198:205], v[154:157]
	v_mfma_f32_16x16x128_f8f6f4 v[142:145], v[18:25], v[206:213], v[142:145]
	v_mfma_f32_16x16x128_f8f6f4 v[138:141], v[26:33], v[206:213], v[138:141]
	v_mfma_f32_16x16x128_f8f6f4 v[126:129], v[18:25], v[214:221], v[126:129]
	v_mfma_f32_16x16x128_f8f6f4 v[122:125], v[26:33], v[214:221], v[122:125]
	v_mfma_f32_16x16x128_f8f6f4 v[110:113], v[18:25], v[222:229], v[110:113]
	v_mfma_f32_16x16x128_f8f6f4 v[106:109], v[26:33], v[222:229], v[106:109]
	s_setprio 0
	s_setprio 1
	v_mfma_f32_16x16x128_f8f6f4 v[150:153], v[2:9], v[198:205], v[150:153]
	v_mfma_f32_16x16x128_f8f6f4 v[146:149], v[10:17], v[198:205], v[146:149]
	v_mfma_f32_16x16x128_f8f6f4 v[134:137], v[2:9], v[206:213], v[134:137]
	v_mfma_f32_16x16x128_f8f6f4 v[130:133], v[10:17], v[206:213], v[130:133]
	v_mfma_f32_16x16x128_f8f6f4 v[118:121], v[2:9], v[214:221], v[118:121]
	v_mfma_f32_16x16x128_f8f6f4 v[114:117], v[10:17], v[214:221], v[114:117]
	v_mfma_f32_16x16x128_f8f6f4 v[102:105], v[2:9], v[222:229], v[102:105]
	v_mfma_f32_16x16x128_f8f6f4 v[98:101], v[10:17], v[222:229], v[98:101]
	s_setprio 0
	s_barrier
	s_mov_b32 m0, s60
	s_mov_b32 s42, s70
	s_mov_b32 s43, s71
	ds_read_b128 v[198:201], v183 offset:16384
	ds_read_b128 v[202:205], v183 offset:17408
	ds_read_b128 v[206:209], v183 offset:18432
	ds_read_b128 v[210:213], v183 offset:19456
	ds_read_b128 v[214:217], v183 offset:20480
	ds_read_b128 v[218:221], v183 offset:21504
	ds_read_b128 v[222:225], v183 offset:22528
	ds_read_b128 v[226:229], v183 offset:23552
	buffer_load_dwordx4 v171, s[40:43], s96 offen lds
	s_mov_b32 m0, s61
	s_add_i32 s0, s96, 0x40000
	buffer_load_dwordx4 v173, s[40:43], s96 offen lds
	s_mov_b32 m0, s62
	s_nop 0
	buffer_load_dwordx4 v171, s[40:43], s0 offen lds
	s_mov_b32 m0, s63
	s_nop 0
	buffer_load_dwordx4 v173, s[40:43], s0 offen lds
	s_waitcnt vmcnt(6)
	s_waitcnt lgkmcnt(0)
	s_barrier
	s_setprio 1
	s_waitcnt lgkmcnt(0)
	v_mfma_f32_16x16x128_f8f6f4 v[94:97], v[18:25], v[198:205], v[94:97]
	v_mfma_f32_16x16x128_f8f6f4 v[90:93], v[26:33], v[198:205], v[90:93]
	v_mfma_f32_16x16x128_f8f6f4 v[78:81], v[18:25], v[206:213], v[78:81]
	v_mfma_f32_16x16x128_f8f6f4 v[74:77], v[26:33], v[206:213], v[74:77]
	v_mfma_f32_16x16x128_f8f6f4 v[62:65], v[18:25], v[214:221], v[62:65]
	v_mfma_f32_16x16x128_f8f6f4 v[58:61], v[26:33], v[214:221], v[58:61]
	v_mfma_f32_16x16x128_f8f6f4 v[46:49], v[18:25], v[222:229], v[46:49]
	v_mfma_f32_16x16x128_f8f6f4 v[42:45], v[26:33], v[222:229], v[42:45]
	s_setprio 0
	s_setprio 1
	v_mfma_f32_16x16x128_f8f6f4 v[86:89], v[2:9], v[198:205], v[86:89]
	v_mfma_f32_16x16x128_f8f6f4 v[82:85], v[10:17], v[198:205], v[82:85]
	v_mfma_f32_16x16x128_f8f6f4 v[70:73], v[2:9], v[206:213], v[70:73]
	v_mfma_f32_16x16x128_f8f6f4 v[66:69], v[10:17], v[206:213], v[66:69]
	v_mfma_f32_16x16x128_f8f6f4 v[54:57], v[2:9], v[214:221], v[54:57]
	v_mfma_f32_16x16x128_f8f6f4 v[50:53], v[10:17], v[214:221], v[50:53]
	v_mfma_f32_16x16x128_f8f6f4 v[38:41], v[2:9], v[222:229], v[38:41]
	v_mfma_f32_16x16x128_f8f6f4 v[34:37], v[10:17], v[222:229], v[34:37]
	s_setprio 0
	s_barrier
	v_add_u32_e32 v14, 0x18000, v181
	v_add_u32_e32 v30, 0x1c000, v181
	ds_read_b128 v[2:5], v14
	ds_read_b128 v[6:9], v14 offset:1024
	ds_read_b128 v[10:13], v14 offset:2048
	ds_read_b128 v[14:17], v14 offset:3072
	ds_read_b128 v[18:21], v30
	ds_read_b128 v[22:25], v30 offset:1024
	ds_read_b128 v[26:29], v30 offset:2048
	ds_read_b128 v[30:33], v30 offset:3072
	s_mov_b32 m0, s65
	ds_read_b128 v[198:201], v183 offset:32768
	ds_read_b128 v[202:205], v183 offset:33792
	ds_read_b128 v[206:209], v183 offset:34816
	ds_read_b128 v[210:213], v183 offset:35840
	ds_read_b128 v[214:217], v183 offset:36864
	ds_read_b128 v[218:221], v183 offset:37888
	ds_read_b128 v[222:225], v183 offset:38912
	ds_read_b128 v[226:229], v183 offset:39936
	s_mov_b32 m0, s59
	s_nop 0
	buffer_load_dwordx4 v192, s[68:71], vcc_lo offen lds
	s_mov_b32 m0, s64
	s_nop 0
	buffer_load_dwordx4 v191, s[68:71], vcc_lo offen lds
	s_mov_b32 m0, s65
	s_nop 0
	buffer_load_dwordx4 v0, s[68:71], vcc_lo offen lds
	s_mov_b32 m0, s66
	s_nop 0
	buffer_load_dwordx4 v193, s[68:71], vcc_lo offen lds
	s_waitcnt vmcnt(8)
	s_waitcnt lgkmcnt(0)
	s_barrier
	s_setprio 1
	s_waitcnt lgkmcnt(0)
	v_mfma_f32_16x16x128_f8f6f4 v[158:161], v[2:9], v[198:205], v[158:161]
	v_mfma_f32_16x16x128_f8f6f4 v[154:157], v[10:17], v[198:205], v[154:157]
	v_mfma_f32_16x16x128_f8f6f4 v[142:145], v[2:9], v[206:213], v[142:145]
	v_mfma_f32_16x16x128_f8f6f4 v[138:141], v[10:17], v[206:213], v[138:141]
	v_mfma_f32_16x16x128_f8f6f4 v[126:129], v[2:9], v[214:221], v[126:129]
	v_mfma_f32_16x16x128_f8f6f4 v[122:125], v[10:17], v[214:221], v[122:125]
	v_mfma_f32_16x16x128_f8f6f4 v[110:113], v[2:9], v[222:229], v[110:113]
	v_mfma_f32_16x16x128_f8f6f4 v[106:109], v[10:17], v[222:229], v[106:109]
	s_setprio 0
	s_setprio 1
	v_mfma_f32_16x16x128_f8f6f4 v[150:153], v[18:25], v[198:205], v[150:153]
	v_mfma_f32_16x16x128_f8f6f4 v[146:149], v[26:33], v[198:205], v[146:149]
	v_mfma_f32_16x16x128_f8f6f4 v[134:137], v[18:25], v[206:213], v[134:137]
	v_mfma_f32_16x16x128_f8f6f4 v[130:133], v[26:33], v[206:213], v[130:133]
	v_mfma_f32_16x16x128_f8f6f4 v[118:121], v[18:25], v[214:221], v[118:121]
	v_mfma_f32_16x16x128_f8f6f4 v[114:117], v[26:33], v[214:221], v[114:117]
	v_mfma_f32_16x16x128_f8f6f4 v[102:105], v[18:25], v[222:229], v[102:105]
	v_mfma_f32_16x16x128_f8f6f4 v[98:101], v[26:33], v[222:229], v[98:101]
	s_setprio 0
	s_barrier
	s_mov_b32 m0, s67
	ds_read_b128 v[198:201], v183 offset:49152
	ds_read_b128 v[202:205], v183 offset:50176
	ds_read_b128 v[206:209], v183 offset:51200
	ds_read_b128 v[210:213], v183 offset:52224
	ds_read_b128 v[214:217], v183 offset:53248
	ds_read_b128 v[218:221], v183 offset:54272
	ds_read_b128 v[222:225], v183 offset:55296
	ds_read_b128 v[226:229], v183 offset:56320
	buffer_load_dwordx4 v171, s[40:43], s97 offen lds
	s_mov_b32 m0, s73
	s_add_i32 s96, s96, 0x40080
	buffer_load_dwordx4 v173, s[40:43], s97 offen lds
	s_mov_b32 m0, s77
	s_nop 0
	buffer_load_dwordx4 v171, s[40:43], s96 offen lds
	s_mov_b32 m0, s78
	s_nop 0
	buffer_load_dwordx4 v173, s[40:43], s96 offen lds
	s_mov_b32 m0, s75
	s_nop 0
	buffer_load_dwordx4 v192, s[68:71], s95 offen lds
	s_mov_b32 m0, s76
	s_nop 0
	buffer_load_dwordx4 v191, s[68:71], s95 offen lds
	s_waitcnt vmcnt(8)
	s_waitcnt lgkmcnt(0)
	s_barrier
	s_setprio 1
	s_waitcnt lgkmcnt(0)
	v_mfma_f32_16x16x128_f8f6f4 v[94:97], v[2:9], v[198:205], v[94:97]
	v_mfma_f32_16x16x128_f8f6f4 v[90:93], v[10:17], v[198:205], v[90:93]
	v_mfma_f32_16x16x128_f8f6f4 v[78:81], v[2:9], v[206:213], v[78:81]
	v_mfma_f32_16x16x128_f8f6f4 v[74:77], v[10:17], v[206:213], v[74:77]
	v_mfma_f32_16x16x128_f8f6f4 v[62:65], v[2:9], v[214:221], v[62:65]
	v_mfma_f32_16x16x128_f8f6f4 v[58:61], v[10:17], v[214:221], v[58:61]
	v_mfma_f32_16x16x128_f8f6f4 v[46:49], v[2:9], v[222:229], v[46:49]
	v_mfma_f32_16x16x128_f8f6f4 v[42:45], v[10:17], v[222:229], v[42:45]
	s_setprio 0
	s_setprio 1
	v_mfma_f32_16x16x128_f8f6f4 v[86:89], v[18:25], v[198:205], v[86:89]
	v_mfma_f32_16x16x128_f8f6f4 v[82:85], v[26:33], v[198:205], v[82:85]
	v_mfma_f32_16x16x128_f8f6f4 v[70:73], v[18:25], v[206:213], v[70:73]
	v_mfma_f32_16x16x128_f8f6f4 v[66:69], v[26:33], v[206:213], v[66:69]
	v_mfma_f32_16x16x128_f8f6f4 v[54:57], v[18:25], v[214:221], v[54:57]
	v_mfma_f32_16x16x128_f8f6f4 v[50:53], v[26:33], v[214:221], v[50:53]
	v_mfma_f32_16x16x128_f8f6f4 v[38:41], v[18:25], v[222:229], v[38:41]
	v_mfma_f32_16x16x128_f8f6f4 v[34:37], v[26:33], v[222:229], v[34:37]
	s_setprio 0
	s_barrier
	s_add_i32 s93, s93, 2
	s_addk_i32 s94, 0x100
	s_cmp_gt_u32 s93, 13
	s_cbranch_scc1 .LBB0_1076

.LBB0_1548:
	s_or_b64 exec, exec, s[46:47]
	v_add_u32_e32 v0, 0x10000, v174
	v_add_u32_e32 v12, 0x14000, v174
	ds_read_b128 v[16:19], v0
	ds_read_b128 v[20:23], v0 offset:1024
	ds_read_b128 v[24:27], v0 offset:2048
	ds_read_b128 v[28:31], v0 offset:3072
	ds_read_b128 v[0:3], v12
	ds_read_b128 v[4:7], v12 offset:1024
	ds_read_b128 v[8:11], v12 offset:2048
	ds_read_b128 v[12:15], v12 offset:3072
	s_add_i32 s92, s88, 0xffffff80
	s_and_b64 s[18:19], s[18:19], exec
	s_cselect_b32 s91, s88, s50
	s_cselect_b32 s47, s87, s51
	s_or_b32 s46, s91, 0x80
	s_or_b32 s90, s47, 0x80
	s_mov_b32 m0, s71
	ds_read_b128 v[176:179], v175
	ds_read_b128 v[180:183], v175 offset:1024
	ds_read_b128 v[184:187], v175 offset:2048
	ds_read_b128 v[188:191], v175 offset:3072
	ds_read_b128 v[198:201], v175 offset:4096
	ds_read_b128 v[202:205], v175 offset:5120
	ds_read_b128 v[206:209], v175 offset:6144
	ds_read_b128 v[210:213], v175 offset:7168
	buffer_load_dwordx4 v167, s[20:23], s92 offen lds
	s_mov_b32 m0, s73
	s_nop 0
	buffer_load_dwordx4 v168, s[20:23], s92 offen lds
	s_waitcnt vmcnt(8)
	s_waitcnt lgkmcnt(0)
	s_barrier
	s_setprio 1
	s_waitcnt lgkmcnt(0)
	v_mfma_f32_16x16x128_f8f6f4 v[156:159], v[16:23], v[176:183], v[156:159]
	v_mfma_f32_16x16x128_f8f6f4 v[152:155], v[24:31], v[176:183], v[152:155]
	v_mfma_f32_16x16x128_f8f6f4 v[140:143], v[16:23], v[184:191], v[140:143]
	v_mfma_f32_16x16x128_f8f6f4 v[136:139], v[24:31], v[184:191], v[136:139]
	v_mfma_f32_16x16x128_f8f6f4 v[124:127], v[16:23], v[198:205], v[124:127]
	v_mfma_f32_16x16x128_f8f6f4 v[120:123], v[24:31], v[198:205], v[120:123]
	v_mfma_f32_16x16x128_f8f6f4 v[108:111], v[16:23], v[206:213], v[108:111]
	v_mfma_f32_16x16x128_f8f6f4 v[104:107], v[24:31], v[206:213], v[104:107]
	s_setprio 0
	s_setprio 1
	v_mfma_f32_16x16x128_f8f6f4 v[148:151], v[0:7], v[176:183], v[148:151]
	v_mfma_f32_16x16x128_f8f6f4 v[144:147], v[8:15], v[176:183], v[144:147]
	v_mfma_f32_16x16x128_f8f6f4 v[132:135], v[0:7], v[184:191], v[132:135]
	v_mfma_f32_16x16x128_f8f6f4 v[128:131], v[8:15], v[184:191], v[128:131]
	v_mfma_f32_16x16x128_f8f6f4 v[116:119], v[0:7], v[198:205], v[116:119]
	v_mfma_f32_16x16x128_f8f6f4 v[112:115], v[8:15], v[198:205], v[112:115]
	v_mfma_f32_16x16x128_f8f6f4 v[100:103], v[0:7], v[206:213], v[100:103]
	v_mfma_f32_16x16x128_f8f6f4 v[96:99], v[8:15], v[206:213], v[96:99]
	s_setprio 0
	s_barrier
	s_mov_b32 m0, s56
	s_mov_b32 s18, s22
	s_mov_b32 s19, s23
	ds_read_b128 v[176:179], v175 offset:16384
	ds_read_b128 v[180:183], v175 offset:17408
	ds_read_b128 v[184:187], v175 offset:18432
	ds_read_b128 v[188:191], v175 offset:19456
	ds_read_b128 v[198:201], v175 offset:20480
	ds_read_b128 v[202:205], v175 offset:21504
	ds_read_b128 v[206:209], v175 offset:22528
	ds_read_b128 v[210:213], v175 offset:23552
	buffer_load_dwordx4 v163, s[16:19], s47 offen lds
	s_mov_b32 m0, s57
	s_add_i32 s92, s47, 0x40000
	buffer_load_dwordx4 v164, s[16:19], s47 offen lds
	s_mov_b32 m0, s58
	s_nop 0
	buffer_load_dwordx4 v163, s[16:19], s92 offen lds
	s_mov_b32 m0, s59
	s_nop 0
	buffer_load_dwordx4 v164, s[16:19], s92 offen lds
	s_waitcnt vmcnt(6)
	s_waitcnt lgkmcnt(0)
	s_barrier
	s_setprio 1
	s_waitcnt lgkmcnt(0)
	v_mfma_f32_16x16x128_f8f6f4 v[92:95], v[16:23], v[176:183], v[92:95]
	v_mfma_f32_16x16x128_f8f6f4 v[88:91], v[24:31], v[176:183], v[88:91]
	v_mfma_f32_16x16x128_f8f6f4 v[76:79], v[16:23], v[184:191], v[76:79]
	v_mfma_f32_16x16x128_f8f6f4 v[64:67], v[24:31], v[184:191], v[64:67]
	v_mfma_f32_16x16x128_f8f6f4 v[48:51], v[16:23], v[198:205], v[48:51]
	v_mfma_f32_16x16x128_f8f6f4 v[44:47], v[24:31], v[198:205], v[44:47]
	v_mfma_f32_16x16x128_f8f6f4 v[36:39], v[16:23], v[206:213], v[36:39]
	v_mfma_f32_16x16x128_f8f6f4 v[32:35], v[24:31], v[206:213], v[32:35]
	s_setprio 0
	s_setprio 1
	v_mfma_f32_16x16x128_f8f6f4 v[84:87], v[0:7], v[176:183], v[84:87]
	v_mfma_f32_16x16x128_f8f6f4 v[68:71], v[8:15], v[176:183], v[68:71]
	v_mfma_f32_16x16x128_f8f6f4 v[52:55], v[0:7], v[184:191], v[52:55]
	v_mfma_f32_16x16x128_f8f6f4 v[40:43], v[8:15], v[184:191], v[40:43]
	v_mfma_f32_16x16x128_f8f6f4 v[72:75], v[0:7], v[198:205], v[72:75]
	v_mfma_f32_16x16x128_f8f6f4 v[80:83], v[8:15], v[198:205], v[80:83]
	v_mfma_f32_16x16x128_f8f6f4 v[56:59], v[0:7], v[206:213], v[56:59]
	v_mfma_f32_16x16x128_f8f6f4 v[60:63], v[8:15], v[206:213], v[60:63]
	s_setprio 0
	s_barrier
	v_add_u32_e32 v12, 0x18000, v174
	v_add_u32_e32 v28, 0x1c000, v174
	ds_read_b128 v[0:3], v12
	ds_read_b128 v[4:7], v12 offset:1024
	ds_read_b128 v[8:11], v12 offset:2048
	ds_read_b128 v[12:15], v12 offset:3072
	ds_read_b128 v[16:19], v28
	ds_read_b128 v[20:23], v28 offset:1024
	ds_read_b128 v[24:27], v28 offset:2048
	ds_read_b128 v[28:31], v28 offset:3072
	s_mov_b32 m0, s61
	ds_read_b128 v[176:179], v175 offset:32768
	ds_read_b128 v[180:183], v175 offset:33792
	ds_read_b128 v[184:187], v175 offset:34816
	ds_read_b128 v[188:191], v175 offset:35840
	ds_read_b128 v[198:201], v175 offset:36864
	ds_read_b128 v[202:205], v175 offset:37888
	ds_read_b128 v[206:209], v175 offset:38912
	ds_read_b128 v[210:213], v175 offset:39936
	s_mov_b32 m0, s55
	s_nop 0
	buffer_load_dwordx4 v165, s[20:23], s91 offen lds
	s_mov_b32 m0, s60
	s_nop 0
	buffer_load_dwordx4 v166, s[20:23], s91 offen lds
	s_mov_b32 m0, s61
	s_nop 0
	buffer_load_dwordx4 v167, s[20:23], s91 offen lds
	s_mov_b32 m0, s62
	s_nop 0
	buffer_load_dwordx4 v168, s[20:23], s91 offen lds
	s_waitcnt vmcnt(8)
	s_waitcnt lgkmcnt(0)
	s_barrier
	s_setprio 1
	s_waitcnt lgkmcnt(0)
	v_mfma_f32_16x16x128_f8f6f4 v[156:159], v[0:7], v[176:183], v[156:159]
	v_mfma_f32_16x16x128_f8f6f4 v[152:155], v[8:15], v[176:183], v[152:155]
	v_mfma_f32_16x16x128_f8f6f4 v[140:143], v[0:7], v[184:191], v[140:143]
	v_mfma_f32_16x16x128_f8f6f4 v[136:139], v[8:15], v[184:191], v[136:139]
	v_mfma_f32_16x16x128_f8f6f4 v[124:127], v[0:7], v[198:205], v[124:127]
	v_mfma_f32_16x16x128_f8f6f4 v[120:123], v[8:15], v[198:205], v[120:123]
	v_mfma_f32_16x16x128_f8f6f4 v[108:111], v[0:7], v[206:213], v[108:111]
	v_mfma_f32_16x16x128_f8f6f4 v[104:107], v[8:15], v[206:213], v[104:107]
	s_setprio 0
	s_setprio 1
	v_mfma_f32_16x16x128_f8f6f4 v[148:151], v[16:23], v[176:183], v[148:151]
	v_mfma_f32_16x16x128_f8f6f4 v[144:147], v[24:31], v[176:183], v[144:147]
	v_mfma_f32_16x16x128_f8f6f4 v[132:135], v[16:23], v[184:191], v[132:135]
	v_mfma_f32_16x16x128_f8f6f4 v[128:131], v[24:31], v[184:191], v[128:131]
	v_mfma_f32_16x16x128_f8f6f4 v[116:119], v[16:23], v[198:205], v[116:119]
	v_mfma_f32_16x16x128_f8f6f4 v[112:115], v[24:31], v[198:205], v[112:115]
	v_mfma_f32_16x16x128_f8f6f4 v[100:103], v[16:23], v[206:213], v[100:103]
	v_mfma_f32_16x16x128_f8f6f4 v[96:99], v[24:31], v[206:213], v[96:99]
	s_setprio 0
	s_barrier
	s_mov_b32 m0, s64
	ds_read_b128 v[176:179], v175 offset:49152
	ds_read_b128 v[180:183], v175 offset:50176
	ds_read_b128 v[184:187], v175 offset:51200
	ds_read_b128 v[188:191], v175 offset:52224
	ds_read_b128 v[198:201], v175 offset:53248
	ds_read_b128 v[202:205], v175 offset:54272
	ds_read_b128 v[206:209], v175 offset:55296
	ds_read_b128 v[210:213], v175 offset:56320
	buffer_load_dwordx4 v163, s[16:19], s90 offen lds
	s_mov_b32 m0, s65
	s_add_i32 s47, s47, 0x40080
	buffer_load_dwordx4 v164, s[16:19], s90 offen lds
	s_mov_b32 m0, s68
	s_nop 0
	buffer_load_dwordx4 v163, s[16:19], s47 offen lds
	s_mov_b32 m0, s69
	s_nop 0
	buffer_load_dwordx4 v164, s[16:19], s47 offen lds
	s_mov_b32 m0, s66
	s_nop 0
	buffer_load_dwordx4 v165, s[20:23], s46 offen lds
	s_mov_b32 m0, s67
	s_nop 0
	buffer_load_dwordx4 v166, s[20:23], s46 offen lds
	s_waitcnt vmcnt(8)
	s_waitcnt lgkmcnt(0)
	s_barrier
	s_setprio 1
	s_waitcnt lgkmcnt(0)
	v_mfma_f32_16x16x128_f8f6f4 v[92:95], v[0:7], v[176:183], v[92:95]
	v_mfma_f32_16x16x128_f8f6f4 v[88:91], v[8:15], v[176:183], v[88:91]
	v_mfma_f32_16x16x128_f8f6f4 v[76:79], v[0:7], v[184:191], v[76:79]
	v_mfma_f32_16x16x128_f8f6f4 v[64:67], v[8:15], v[184:191], v[64:67]
	v_mfma_f32_16x16x128_f8f6f4 v[48:51], v[0:7], v[198:205], v[48:51]
	v_mfma_f32_16x16x128_f8f6f4 v[44:47], v[8:15], v[198:205], v[44:47]
	v_mfma_f32_16x16x128_f8f6f4 v[36:39], v[0:7], v[206:213], v[36:39]
	v_mfma_f32_16x16x128_f8f6f4 v[32:35], v[8:15], v[206:213], v[32:35]
	s_setprio 0
	s_setprio 1
	v_mfma_f32_16x16x128_f8f6f4 v[84:87], v[16:23], v[176:183], v[84:87]
	v_mfma_f32_16x16x128_f8f6f4 v[68:71], v[24:31], v[176:183], v[68:71]
	v_mfma_f32_16x16x128_f8f6f4 v[52:55], v[16:23], v[184:191], v[52:55]
	v_mfma_f32_16x16x128_f8f6f4 v[40:43], v[24:31], v[184:191], v[40:43]
	v_mfma_f32_16x16x128_f8f6f4 v[72:75], v[16:23], v[198:205], v[72:75]
	v_mfma_f32_16x16x128_f8f6f4 v[80:83], v[24:31], v[198:205], v[80:83]
	v_mfma_f32_16x16x128_f8f6f4 v[56:59], v[16:23], v[206:213], v[56:59]
	v_mfma_f32_16x16x128_f8f6f4 v[60:63], v[24:31], v[206:213], v[60:63]
	s_setprio 0
	s_barrier
	s_add_i32 s89, s89, 2
	s_addk_i32 s87, 0x100
	s_addk_i32 s88, 0x100
	s_cmp_gt_u32 s89, 13
	s_cbranch_scc1 .LBB0_1551
